# v83 plus DPP/permlane-swap reductions for the norm2 row-pair max and the oq row max
# baseline (speedup 1.0000x reference)
; __device__ __forceinline__ float bflo(unsigned w) { return __uint_as_float(w << 16); }
; __device__ __forceinline__ float bfhi(unsigned w) { return __uint_as_float(w & 0xffff0000u); }
; __device__ __forceinline__ unsigned pack_i8x4(float a, float b, float c, float d, float inv) { return q8u(a, inv) | (q8u(b, inv) << 8) | (q8u(c, inv) << 16) | (q8u(d, inv) << 24); }
; __device__ __forceinline__ float wave_max(float v) {
; #pragma unroll
;     for (int o = 1; o < 64; o <<= 1) v = fmaxf(v, __shfl_xor(v, o));
;     return v;
; __device__ __forceinline__ void phase_oq(const Params& p, const Ctx& F, const int l) {
;     for (int R = F.gw; R < NROWS; R += F.NGW) {
;         if (l == 1 && (R % TPB) < CTXL) continue;
;         const bf16_t* src = F.r1 + (size_t)R * DM + 8 * F.lane;
;         u32x4 w[4];
; #pragma unroll
;         for (int j = 0; j < 4; ++j) w[j] = __builtin_nontemporal_load((const u32x4*)(src + 512 * j));
;         float v[4][8], am = 0.f;
; #pragma unroll
;         for (int j = 0; j < 4; ++j) { v[j][0] = bflo(w[j].x); v[j][1] = bfhi(w[j].x); v[j][2] = bflo(w[j].y); v[j][3] = bfhi(w[j].y); v[j][4] = bflo(w[j].z); v[j][5] = bfhi(w[j].z); v[j][6] = bflo(w[j].w); v[j][7] = bfhi(w[j].w);
; #pragma unroll
;             for (int q = 0; q < 8; ++q) am = fmaxf(am, fabsf(v[j][q])); }
;         am = fmaxf(wave_max(am), 1e-20f); const float inv = 127.f / am;
;         signed char* dst = F.o8 + (size_t)R * DM + 8 * F.lane;
; #pragma unroll
;         for (int j = 0; j < 4; ++j) { u32x2 o; o.x = pack_i8x4(v[j][0], v[j][1], v[j][2], v[j][3], inv); o.y = pack_i8x4(v[j][4], v[j][5], v[j][6], v[j][7], inv); *(u32x2*)(dst + 512 * j) = o; }
.LBB0_739:
	global_load_dwordx4 v[12:15], v[4:5], off offset:-2048 nt
	global_load_dwordx4 v[16:19], v[4:5], off offset:-1024 nt
	global_load_dwordx4 v[20:23], v[4:5], off nt
	global_load_dwordx4 v[24:27], v[4:5], off offset:1024 nt
	s_waitcnt vmcnt(0)
	v_lshlrev_b32_e32 v1, 16, v12
	v_and_b32_e32 v28, 0xffff0000, v12
	v_lshlrev_b32_e32 v29, 16, v13
	v_and_b32_e32 v13, 0xffff0000, v13
	v_max3_f32 v12, |v1|, 0, |v28|
	v_lshlrev_b32_e32 v30, 16, v14
	v_and_b32_e32 v14, 0xffff0000, v14
	v_max3_f32 v12, v12, |v29|, |v13|
	v_lshlrev_b32_e32 v31, 16, v15
	v_and_b32_e32 v15, 0xffff0000, v15
	v_max3_f32 v12, v12, |v30|, |v14|
	v_lshlrev_b32_e32 v32, 16, v16
	v_and_b32_e32 v16, 0xffff0000, v16
	v_max3_f32 v12, v12, |v31|, |v15|
	v_lshlrev_b32_e32 v33, 16, v17
	v_and_b32_e32 v17, 0xffff0000, v17
	v_max3_f32 v12, v12, |v32|, |v16|
	v_lshlrev_b32_e32 v34, 16, v18
	v_and_b32_e32 v18, 0xffff0000, v18
	v_max3_f32 v12, v12, |v33|, |v17|
	v_lshlrev_b32_e32 v36, 16, v19
	v_and_b32_e32 v19, 0xffff0000, v19
	v_max3_f32 v12, v12, |v34|, |v18|
	v_lshlrev_b32_e32 v37, 16, v20
	v_and_b32_e32 v20, 0xffff0000, v20
	v_max3_f32 v12, v12, |v36|, |v19|
	v_lshlrev_b32_e32 v38, 16, v21
	v_and_b32_e32 v21, 0xffff0000, v21
	v_max3_f32 v12, v12, |v37|, |v20|
	v_lshlrev_b32_e32 v39, 16, v22
	v_and_b32_e32 v22, 0xffff0000, v22
	v_max3_f32 v12, v12, |v38|, |v21|
	v_lshlrev_b32_e32 v40, 16, v23
	v_and_b32_e32 v23, 0xffff0000, v23
	v_max3_f32 v12, v12, |v39|, |v22|
	v_lshlrev_b32_e32 v41, 16, v24
	v_and_b32_e32 v24, 0xffff0000, v24
	v_max3_f32 v12, v12, |v40|, |v23|
	v_lshlrev_b32_e32 v42, 16, v25
	v_and_b32_e32 v25, 0xffff0000, v25
	v_max3_f32 v12, v12, |v41|, |v24|
	v_lshlrev_b32_e32 v43, 16, v26
	v_and_b32_e32 v26, 0xffff0000, v26
	v_max3_f32 v12, v12, |v42|, |v25|
	v_lshlrev_b32_e32 v44, 16, v27
	v_and_b32_e32 v27, 0xffff0000, v27
	v_max3_f32 v12, v12, |v43|, |v26|
	v_max3_f32 v12, v12, |v44|, |v27|
	s_nop 1
	v_max_f32_dpp v12, v12, v12 quad_perm:[1,0,3,2] row_mask:0xf bank_mask:0xf
	s_nop 1
	v_max_f32_dpp v12, v12, v12 quad_perm:[2,3,0,1] row_mask:0xf bank_mask:0xf
	s_nop 1
	v_max_f32_dpp v12, v12, v12 row_half_mirror row_mask:0xf bank_mask:0xf
	s_nop 1
	v_max_f32_dpp v12, v12, v12 row_mirror row_mask:0xf bank_mask:0xf
	v_mov_b32_e32 v45, v12
	s_nop 1
	v_permlane16_swap_b32_e32 v12, v45
	v_max_f32_e32 v12, v12, v45
	v_mov_b32_e32 v45, v12
	s_nop 1
	v_permlane32_swap_b32_e32 v12, v45
	v_max3_f32 v12, v12, v45, s53
	v_div_scale_f32 v45, s[12:13], v12, v12, s54
	v_rcp_f32_e32 v46, v45
	v_div_scale_f32 v47, vcc, s54, v12, s54
	v_fma_f32 v48, -v45, v46, 1.0
	v_fmac_f32_e32 v46, v48, v46
	v_mul_f32_e32 v48, v47, v46
	v_fma_f32 v49, -v45, v48, v47
	v_fmac_f32_e32 v48, v49, v46
	v_fma_f32 v45, -v45, v48, v47
	v_div_fmas_f32 v45, v45, v46, v48
	v_div_fixup_f32 v45, v45, v12, s54
	v_mul_f32_e32 v1, v45, v1
	v_mul_f32_e32 v13, v45, v13
	v_mul_f32_e32 v14, v45, v14
	v_mul_f32_e32 v31, v45, v31
	v_mul_f32_e32 v28, v45, v28
	v_mul_f32_e32 v29, v45, v29
	v_mul_f32_e32 v30, v45, v30
	v_mul_f32_e32 v15, v45, v15
	v_rndne_f32_e32 v1, v1
	v_rndne_f32_e32 v13, v13
	v_rndne_f32_e32 v14, v14
	v_rndne_f32_e32 v31, v31
	v_rndne_f32_e32 v28, v28
	v_rndne_f32_e32 v29, v29
	v_rndne_f32_e32 v30, v30
	v_rndne_f32_e32 v15, v15
	v_cvt_i32_f32_e32 v1, v1
	v_cvt_i32_f32_e32 v13, v13
	v_cvt_i32_f32_e32 v14, v14
	v_cvt_i32_f32_e32 v31, v31
	v_cvt_i32_f32_e32 v28, v28
	v_cvt_i32_f32_e32 v29, v29
	v_cvt_i32_f32_e32 v30, v30
	v_cvt_i32_f32_e32 v15, v15
	v_med3_i32 v1, v1, s80, v218
	v_med3_i32 v13, v13, s80, v218
	v_med3_i32 v14, v14, s80, v218
	v_med3_i32 v31, v31, s80, v218
	v_med3_i32 v28, v28, s80, v218
	v_med3_i32 v29, v29, s80, v218
	v_med3_i32 v30, v30, s80, v218
	v_med3_i32 v15, v15, s80, v218
	v_perm_b32 v1, v13, v1, s81
	v_lshlrev_b32_e32 v13, 8, v14
	v_lshlrev_b32_e32 v14, 16, v31
	v_mul_f32_e32 v16, v45, v16
	v_mul_f32_e32 v33, v45, v33
	v_mul_f32_e32 v18, v45, v18
	v_mul_f32_e32 v36, v45, v36
	v_lshlrev_b32_e32 v28, 8, v28
	v_lshlrev_b32_e32 v29, 16, v29
	v_perm_b32 v15, v15, v30, s81
	v_and_b32_e32 v13, 0xff00, v13
	v_and_b32_e32 v31, 0xff0000, v14
	v_mul_f32_e32 v32, v45, v32
	v_mul_f32_e32 v17, v45, v17
	v_mul_f32_e32 v34, v45, v34
; __device__ __forceinline__ unsigned pack_i8x4(float a, float b, float c, float d, float inv) { return q8u(a, inv) | (q8u(b, inv) << 8) | (q8u(c, inv) << 16) | (q8u(d, inv) << 24); }
; __device__ __forceinline__ void phase_oq(const Params& p, const Ctx& F, const int l) {
;     ...
;         signed char* dst = F.o8 + (size_t)R * DM + 8 * F.lane;
; #pragma unroll
;         for (int j = 0; j < 4; ++j) { u32x2 o; o.x = pack_i8x4(v[j][0], v[j][1], v[j][2], v[j][3], inv); o.y = pack_i8x4(v[j][4], v[j][5], v[j][6], v[j][7], inv); *(u32x2*)(dst + 512 * j) = o; }
;         if (F.lane == 0) F.so[R] = am * (1.f / 127.f);
	v_rndne_f32_e32 v16, v16
	v_rndne_f32_e32 v33, v33
	v_rndne_f32_e32 v18, v18
	v_rndne_f32_e32 v36, v36
	v_and_b32_e32 v28, 0xff00, v28
	v_and_b32_e32 v29, 0xff0000, v29
	v_or3_b32 v15, v15, v13, v31
	v_mul_f32_e32 v13, v45, v19
	v_rndne_f32_e32 v32, v32
	v_rndne_f32_e32 v17, v17
	v_rndne_f32_e32 v34, v34
	v_cvt_i32_f32_e32 v16, v16
	v_cvt_i32_f32_e32 v33, v33
	v_cvt_i32_f32_e32 v18, v18
	v_or3_b32 v14, v1, v28, v29
	v_cvt_i32_f32_e32 v1, v36
	v_rndne_f32_e32 v13, v13
	v_cvt_i32_f32_e32 v32, v32
	v_cvt_i32_f32_e32 v17, v17
	v_cvt_i32_f32_e32 v34, v34
	global_store_dwordx2 v[2:3], v[14:15], off offset:-1024
	v_cvt_i32_f32_e32 v13, v13
	v_mul_f32_e32 v14, v45, v37
	v_rndne_f32_e32 v14, v14
	v_mul_f32_e32 v15, v45, v20
	v_cvt_i32_f32_e32 v14, v14
	v_rndne_f32_e32 v15, v15
	v_med3_i32 v16, v16, s80, v218
	v_med3_i32 v33, v33, s80, v218
	v_med3_i32 v18, v18, s80, v218
	v_med3_i32 v1, v1, s80, v218
	v_cvt_i32_f32_e32 v15, v15
	v_med3_i32 v32, v32, s80, v218
	v_med3_i32 v17, v17, s80, v218
	v_med3_i32 v34, v34, s80, v218
	v_lshlrev_b32_e32 v16, 8, v16
	v_lshlrev_b32_e32 v30, 16, v33
	v_lshlrev_b32_e32 v18, 8, v18
	v_lshlrev_b32_e32 v1, 16, v1
	v_med3_i32 v13, v13, s80, v218
	v_perm_b32 v17, v17, v32, s81
	v_and_b32_e32 v16, 0xff00, v16
	v_and_b32_e32 v30, 0xff0000, v30
	v_and_b32_e32 v18, 0xff00, v18
	v_and_b32_e32 v1, 0xff0000, v1
	v_perm_b32 v13, v13, v34, s81
	v_or3_b32 v16, v17, v16, v30
	v_or3_b32 v17, v13, v18, v1
	v_med3_i32 v1, v14, s80, v218
	v_mul_f32_e32 v14, v45, v38
	v_med3_i32 v13, v15, s80, v218
	v_rndne_f32_e32 v14, v14
	v_mul_f32_e32 v15, v45, v21
	v_cvt_i32_f32_e32 v14, v14
	v_rndne_f32_e32 v15, v15
	global_store_dwordx2 v[2:3], v[16:17], off offset:-512
	v_cvt_i32_f32_e32 v15, v15
	v_mul_f32_e32 v16, v45, v39
	v_rndne_f32_e32 v16, v16
	v_cvt_i32_f32_e32 v16, v16
	v_med3_i32 v14, v14, s80, v218
	v_lshlrev_b32_e32 v13, 8, v13
	v_lshlrev_b32_e32 v14, 16, v14
	v_med3_i32 v15, v15, s80, v218
	v_and_b32_e32 v13, 0xff00, v13
	v_and_b32_e32 v14, 0xff0000, v14
	v_perm_b32 v1, v15, v1, s81
	v_mul_f32_e32 v17, v45, v22
	v_or3_b32 v14, v1, v13, v14
	v_med3_i32 v1, v16, s80, v218
	v_mul_f32_e32 v15, v45, v40
	v_mul_f32_e32 v16, v45, v23
	v_rndne_f32_e32 v17, v17
	v_rndne_f32_e32 v15, v15
	v_rndne_f32_e32 v16, v16
	v_cvt_i32_f32_e32 v17, v17
	v_cvt_i32_f32_e32 v15, v15
	v_cvt_i32_f32_e32 v16, v16
	v_med3_i32 v13, v17, s80, v218
	v_med3_i32 v15, v15, s80, v218
	v_med3_i32 v16, v16, s80, v218
	v_lshlrev_b32_e32 v13, 8, v13
	v_lshlrev_b32_e32 v15, 16, v15
	v_perm_b32 v1, v16, v1, s81
	v_mul_f32_e32 v16, v45, v41
	v_and_b32_e32 v13, 0xff00, v13
	v_and_b32_e32 v15, 0xff0000, v15
	v_rndne_f32_e32 v16, v16
	v_cvt_i32_f32_e32 v16, v16
	v_or3_b32 v15, v1, v13, v15
	v_mul_f32_e32 v17, v45, v24
	global_store_dwordx2 v[2:3], v[14:15], off
	v_mul_f32_e32 v14, v45, v42
	v_rndne_f32_e32 v17, v17
	v_rndne_f32_e32 v14, v14
	v_mul_f32_e32 v15, v45, v25
	v_cvt_i32_f32_e32 v17, v17
	v_cvt_i32_f32_e32 v14, v14
	v_rndne_f32_e32 v15, v15
	v_med3_i32 v1, v16, s80, v218
	v_cvt_i32_f32_e32 v15, v15
	v_mul_f32_e32 v16, v45, v43
	v_rndne_f32_e32 v16, v16
	v_cvt_i32_f32_e32 v16, v16
	v_med3_i32 v13, v17, s80, v218
	v_med3_i32 v14, v14, s80, v218
	v_lshlrev_b32_e32 v13, 8, v13
	v_lshlrev_b32_e32 v14, 16, v14
	v_med3_i32 v15, v15, s80, v218
	v_and_b32_e32 v13, 0xff00, v13
	v_and_b32_e32 v14, 0xff0000, v14
	v_mul_f32_e32 v17, v45, v26
	v_perm_b32 v1, v15, v1, s81
	v_mul_f32_e32 v15, v45, v44
	v_rndne_f32_e32 v17, v17
	v_or3_b32 v14, v1, v13, v14
	v_med3_i32 v1, v16, s80, v218
	v_rndne_f32_e32 v15, v15
	v_mul_f32_e32 v16, v45, v27
	v_cvt_i32_f32_e32 v17, v17
	v_cvt_i32_f32_e32 v15, v15
	v_rndne_f32_e32 v16, v16
	v_cvt_i32_f32_e32 v16, v16
	v_med3_i32 v13, v17, s80, v218
	v_med3_i32 v15, v15, s80, v218
	v_lshlrev_b32_e32 v13, 8, v13
	v_lshlrev_b32_e32 v15, 16, v15
	v_med3_i32 v16, v16, s80, v218
	v_and_b32_e32 v13, 0xff00, v13
	v_and_b32_e32 v15, 0xff0000, v15
	v_perm_b32 v1, v16, v1, s81
	v_or3_b32 v15, v1, v13, v15
	global_store_dwordx2 v[2:3], v[14:15], off offset:512
	s_and_saveexec_b64 s[12:13], s[0:1]
	s_cbranch_execz .LBB0_738
	v_mul_f32_e32 v1, 0x3c010204, v12
	global_store_dword v35, v1, s[4:5]
	s_branch .LBB0_738

; __device__ __forceinline__ float bflo(unsigned w) { return __uint_as_float(w << 16); }
; __device__ __forceinline__ float bfhi(unsigned w) { return __uint_as_float(w & 0xffff0000u); }
; __device__ __forceinline__ void phase_norm2(const Params& p, const Ctx& F, const int l) {
;     ...
;         { const float* xlat = l == 0 ? p.x : p.out; const float* xctx = l == 0 ? p.ctx : F.xc;
;           const float* xs0 = isctx ? xctx + ((size_t)b * CTXL + t) * DM : xlat + ((size_t)b * SEQ + (t - CTXL)) * DM;
;           const float* xs1 = two ? xlat + ((size_t)b * SEQ + (tB - CTXL)) * DM : xs0;
;           const bf16_t* d0p = F.dlt + ((size_t)b * TPB + t) * DM + 4 * F.lane; const bf16_t* d1p = F.dlt + ((size_t)b * TPB + (two ? tB : t)) * DM + 4 * F.lane;
; #pragma unroll
;           for (int j = 0; j < 8; ++j) { f32x4 x0 = __builtin_nontemporal_load((const f32x4*)xs0 + F.lane + 64 * j), x1 = __builtin_nontemporal_load((const f32x4*)xs1 + F.lane + 64 * j);
;               const u32x2 e0 = __builtin_nontemporal_load((const u32x2*)(d0p + 256 * j)), e1 = __builtin_nontemporal_load((const u32x2*)(d1p + 256 * j));
;               x0 += (f32x4){bflo(e0.x), bfhi(e0.x), bflo(e0.y), bfhi(e0.y)}; x1 += (f32x4){bflo(e1.x), bfhi(e1.x), bflo(e1.y), bfhi(e1.y)};
; #pragma unroll
;               for (int c = 0; c < 4; ++c) vv[j][c] = (f32x2){x0[c], x1[c]}; } }
.LBB0_918:
	s_waitcnt vmcnt(19)
	v_lshlrev_b32_e32 v185, 16, v182
	v_lshlrev_b32_e32 v184, 16, v180
	v_mov_b32_e32 v186, v124
	v_mov_b32_e32 v187, v128
	v_pk_add_f32 v[184:185], v[186:187], v[184:185]
	v_and_b32_e32 v187, 0xffff0000, v182
	v_and_b32_e32 v186, 0xffff0000, v180
	v_mov_b32_e32 v128, v125
	v_pk_add_f32 v[128:129], v[128:129], v[186:187]
	v_lshlrev_b32_e32 v125, 16, v183
	v_lshlrev_b32_e32 v124, 16, v181
	v_mov_b32_e32 v186, v126
	v_mov_b32_e32 v187, v130
	v_pk_add_f32 v[186:187], v[186:187], v[124:125]
	v_and_b32_e32 v125, 0xffff0000, v183
	v_and_b32_e32 v124, 0xffff0000, v181
	v_mov_b32_e32 v130, v127
	v_pk_add_f32 v[130:131], v[130:131], v[124:125]
	s_waitcnt vmcnt(18)
	v_lshlrev_b32_e32 v125, 16, v178
	v_lshlrev_b32_e32 v124, 16, v176
	v_mov_b32_e32 v126, v116
	v_mov_b32_e32 v127, v120
	v_pk_add_f32 v[180:181], v[126:127], v[124:125]
	v_and_b32_e32 v125, 0xffff0000, v178
	v_and_b32_e32 v124, 0xffff0000, v176
	v_mov_b32_e32 v120, v117
	v_pk_add_f32 v[116:117], v[120:121], v[124:125]
	v_lshlrev_b32_e32 v121, 16, v179
	v_lshlrev_b32_e32 v120, 16, v177
	v_mov_b32_e32 v124, v118
	v_mov_b32_e32 v125, v122
	v_pk_add_f32 v[120:121], v[124:125], v[120:121]
	v_and_b32_e32 v125, 0xffff0000, v179
	v_and_b32_e32 v124, 0xffff0000, v177
	v_mov_b32_e32 v122, v119
	v_pk_add_f32 v[122:123], v[122:123], v[124:125]
	s_waitcnt vmcnt(17)
	v_lshlrev_b32_e32 v119, 16, v174
	v_lshlrev_b32_e32 v118, 16, v172
	v_mov_b32_e32 v124, v108
	v_mov_b32_e32 v125, v112
	v_pk_add_f32 v[176:177], v[124:125], v[118:119]
	v_and_b32_e32 v119, 0xffff0000, v174
	v_and_b32_e32 v118, 0xffff0000, v172
	v_mov_b32_e32 v112, v109
	v_pk_add_f32 v[178:179], v[112:113], v[118:119]
	v_lshlrev_b32_e32 v109, 16, v175
	v_lshlrev_b32_e32 v108, 16, v173
	v_mov_b32_e32 v112, v110
	v_mov_b32_e32 v113, v114
	v_pk_add_f32 v[182:183], v[112:113], v[108:109]
	v_and_b32_e32 v109, 0xffff0000, v175
	v_and_b32_e32 v108, 0xffff0000, v173
	v_mov_b32_e32 v114, v111
	v_pk_add_f32 v[172:173], v[114:115], v[108:109]
	s_waitcnt vmcnt(16)
	v_lshlrev_b32_e32 v109, 16, v168
	v_lshlrev_b32_e32 v108, 16, v164
	v_mov_b32_e32 v110, v100
	v_mov_b32_e32 v111, v104
	v_pk_add_f32 v[174:175], v[110:111], v[108:109]
	v_and_b32_e32 v109, 0xffff0000, v168
	v_and_b32_e32 v108, 0xffff0000, v164
	v_mov_b32_e32 v104, v101
	v_pk_add_f32 v[100:101], v[104:105], v[108:109]
	v_lshlrev_b32_e32 v105, 16, v169
	v_lshlrev_b32_e32 v104, 16, v165
	v_mov_b32_e32 v108, v102
	v_mov_b32_e32 v109, v106
	v_pk_add_f32 v[104:105], v[108:109], v[104:105]
	v_and_b32_e32 v109, 0xffff0000, v169
	v_and_b32_e32 v108, 0xffff0000, v165
	v_mov_b32_e32 v106, v103
	v_pk_add_f32 v[106:107], v[106:107], v[108:109]
	s_waitcnt vmcnt(3)
	v_lshlrev_b32_e32 v103, 16, v170
	v_lshlrev_b32_e32 v102, 16, v166
	v_mov_b32_e32 v108, v92
	v_mov_b32_e32 v109, v96
	v_pk_add_f32 v[164:165], v[108:109], v[102:103]
	v_and_b32_e32 v103, 0xffff0000, v170
	v_and_b32_e32 v102, 0xffff0000, v166
	v_mov_b32_e32 v96, v93
	v_pk_add_f32 v[168:169], v[96:97], v[102:103]
	v_lshlrev_b32_e32 v93, 16, v171
	v_lshlrev_b32_e32 v92, 16, v167
	v_mov_b32_e32 v96, v94
	v_mov_b32_e32 v97, v98
	v_pk_add_f32 v[188:189], v[96:97], v[92:93]
	v_and_b32_e32 v93, 0xffff0000, v171
	v_and_b32_e32 v92, 0xffff0000, v167
	v_mov_b32_e32 v98, v95
	v_pk_add_f32 v[166:167], v[98:99], v[92:93]
	s_waitcnt vmcnt(2)
	v_lshlrev_b32_e32 v93, 16, v162
	v_lshlrev_b32_e32 v92, 16, v160
	v_mov_b32_e32 v94, v84
	v_mov_b32_e32 v95, v88
	v_pk_add_f32 v[170:171], v[94:95], v[92:93]
	v_and_b32_e32 v93, 0xffff0000, v162
	v_and_b32_e32 v92, 0xffff0000, v160
	v_mov_b32_e32 v88, v85
	v_pk_add_f32 v[84:85], v[88:89], v[92:93]
	v_lshlrev_b32_e32 v89, 16, v163
	v_lshlrev_b32_e32 v88, 16, v161
	v_mov_b32_e32 v92, v86
	v_mov_b32_e32 v93, v90
	v_pk_add_f32 v[88:89], v[92:93], v[88:89]
	v_and_b32_e32 v93, 0xffff0000, v163
	v_and_b32_e32 v92, 0xffff0000, v161
	v_mov_b32_e32 v90, v87
	v_pk_add_f32 v[90:91], v[90:91], v[92:93]
	s_waitcnt vmcnt(1)
	v_lshlrev_b32_e32 v87, 16, v158
	v_lshlrev_b32_e32 v86, 16, v156
	v_mov_b32_e32 v92, v76
	v_mov_b32_e32 v93, v80
	v_pk_add_f32 v[160:161], v[92:93], v[86:87]
	v_and_b32_e32 v87, 0xffff0000, v158
	v_and_b32_e32 v86, 0xffff0000, v156
	v_mov_b32_e32 v80, v77
	v_pk_add_f32 v[162:163], v[80:81], v[86:87]
	v_lshlrev_b32_e32 v77, 16, v159
	v_lshlrev_b32_e32 v76, 16, v157
	v_mov_b32_e32 v80, v78
	v_mov_b32_e32 v81, v82
	v_pk_add_f32 v[198:199], v[80:81], v[76:77]
	v_and_b32_e32 v77, 0xffff0000, v159
	v_and_b32_e32 v76, 0xffff0000, v157
	v_mov_b32_e32 v82, v79
	v_pk_add_f32 v[156:157], v[82:83], v[76:77]
	s_waitcnt vmcnt(0)
; __device__ __forceinline__ float wave_sum(float v) {
; #pragma unroll
;     for (int o = 1; o < 64; o <<= 1) v += __shfl_xor(v, o);
;     return v;
; __device__ __forceinline__ void phase_norm2(const Params& p, const Ctx& F, const int l) {
;     ...
;         f32x2 ss = {0.f, 0.f};
; #pragma unroll
;         for (int j = 0; j < 8; ++j)
; #pragma unroll
;             for (int c = 0; c < 4; ++c) ss += vv[j][c] * vv[j][c];
;         const f32x2 rstd = {rsqrtf(wave_sum(ss.x) * (1.f / DM) + EPS), rsqrtf(wave_sum(ss.y) * (1.f / DM) + EPS)};
;         f32x2 am = {0.f, 0.f};
; #pragma unroll
;         for (int j = 0; j < 8; ++j)
; #pragma unroll
;             for (int c = 0; c < 4; ++c) { vv[j][c] = vv[j][c] * rstd * A[j][c] + Bv[j][c]; am = __builtin_elementwise_max(am, __builtin_elementwise_abs(vv[j][c])); }
	v_lshlrev_b32_e32 v77, 16, v154
	v_lshlrev_b32_e32 v76, 16, v152
	v_mov_b32_e32 v78, v68
	v_mov_b32_e32 v79, v72
	v_pk_add_f32 v[158:159], v[78:79], v[76:77]
	v_and_b32_e32 v77, 0xffff0000, v154
	v_and_b32_e32 v76, 0xffff0000, v152
	v_mov_b32_e32 v72, v69
	v_pk_add_f32 v[72:73], v[72:73], v[76:77]
	v_lshlrev_b32_e32 v69, 16, v155
	v_lshlrev_b32_e32 v68, 16, v153
	v_mov_b32_e32 v76, v70
	v_mov_b32_e32 v77, v74
	v_pk_add_f32 v[200:201], v[76:77], v[68:69]
	v_and_b32_e32 v69, 0xffff0000, v155
	v_and_b32_e32 v68, 0xffff0000, v153
	v_mov_b32_e32 v74, v71
	v_pk_add_f32 v[74:75], v[74:75], v[68:69]
	v_pk_mul_f32 v[68:69], v[128:129], v[128:129]
	s_mov_b32 s0, 0x3a000000
	v_pk_fma_f32 v[68:69], v[184:185], v[184:185], v[68:69]
	s_mov_b32 s30, 0x45800000
	v_pk_fma_f32 v[68:69], v[186:187], v[186:187], v[68:69]
	v_mov_b32_e32 v34, v9
	v_pk_fma_f32 v[68:69], v[130:131], v[130:131], v[68:69]
	s_mov_b32 s52, 0x800000
	v_pk_fma_f32 v[68:69], v[180:181], v[180:181], v[68:69]
	s_nop 0
	v_pk_fma_f32 v[68:69], v[116:117], v[116:117], v[68:69]
	s_nop 0
	v_pk_fma_f32 v[68:69], v[120:121], v[120:121], v[68:69]
	s_nop 0
	v_pk_fma_f32 v[68:69], v[122:123], v[122:123], v[68:69]
	s_nop 0
	v_pk_fma_f32 v[68:69], v[176:177], v[176:177], v[68:69]
	s_nop 0
	v_pk_fma_f32 v[68:69], v[178:179], v[178:179], v[68:69]
	s_nop 0
	v_pk_fma_f32 v[68:69], v[182:183], v[182:183], v[68:69]
	s_nop 0
	v_pk_fma_f32 v[68:69], v[172:173], v[172:173], v[68:69]
	s_nop 0
	v_pk_fma_f32 v[68:69], v[174:175], v[174:175], v[68:69]
	s_nop 0
	v_pk_fma_f32 v[68:69], v[100:101], v[100:101], v[68:69]
	s_nop 0
	v_pk_fma_f32 v[68:69], v[104:105], v[104:105], v[68:69]
	s_nop 0
	v_pk_fma_f32 v[68:69], v[106:107], v[106:107], v[68:69]
	s_nop 0
	v_pk_fma_f32 v[68:69], v[164:165], v[164:165], v[68:69]
	s_nop 0
	v_pk_fma_f32 v[68:69], v[168:169], v[168:169], v[68:69]
	s_nop 0
	v_pk_fma_f32 v[68:69], v[188:189], v[188:189], v[68:69]
	s_nop 0
	v_pk_fma_f32 v[68:69], v[166:167], v[166:167], v[68:69]
	s_nop 0
	v_pk_fma_f32 v[68:69], v[170:171], v[170:171], v[68:69]
	s_nop 0
	v_pk_fma_f32 v[68:69], v[84:85], v[84:85], v[68:69]
	s_nop 0
	v_pk_fma_f32 v[68:69], v[88:89], v[88:89], v[68:69]
	s_nop 0
	v_pk_fma_f32 v[68:69], v[90:91], v[90:91], v[68:69]
	s_nop 0
	v_pk_fma_f32 v[68:69], v[160:161], v[160:161], v[68:69]
	s_nop 0
	v_pk_fma_f32 v[68:69], v[162:163], v[162:163], v[68:69]
	s_nop 0
	v_pk_fma_f32 v[68:69], v[198:199], v[198:199], v[68:69]
	s_nop 0
	v_pk_fma_f32 v[68:69], v[156:157], v[156:157], v[68:69]
	s_nop 0
	v_pk_fma_f32 v[68:69], v[158:159], v[158:159], v[68:69]
	s_nop 0
	v_pk_fma_f32 v[68:69], v[72:73], v[72:73], v[68:69]
	s_nop 0
	v_pk_fma_f32 v[68:69], v[200:201], v[200:201], v[68:69]
	s_nop 0
	v_pk_fma_f32 v[68:69], v[74:75], v[74:75], v[68:69]
	s_nop 1
	v_add_f32_dpp v68, v68, v68 quad_perm:[1,0,3,2] row_mask:0xf bank_mask:0xf
	v_add_f32_dpp v69, v69, v69 quad_perm:[1,0,3,2] row_mask:0xf bank_mask:0xf
	s_nop 1
	v_add_f32_dpp v68, v68, v68 quad_perm:[2,3,0,1] row_mask:0xf bank_mask:0xf
	v_add_f32_dpp v69, v69, v69 quad_perm:[2,3,0,1] row_mask:0xf bank_mask:0xf
	s_nop 1
	v_add_f32_dpp v68, v68, v68 row_half_mirror row_mask:0xf bank_mask:0xf
	v_add_f32_dpp v69, v69, v69 row_half_mirror row_mask:0xf bank_mask:0xf
	s_nop 1
	v_add_f32_dpp v68, v68, v68 row_mirror row_mask:0xf bank_mask:0xf
	v_add_f32_dpp v69, v69, v69 row_mirror row_mask:0xf bank_mask:0xf
	v_mov_b32_e32 v70, v68
	v_mov_b32_e32 v71, v69
	s_nop 1
	v_permlane16_swap_b32_e32 v68, v70
	v_permlane16_swap_b32_e32 v69, v71
	v_add_f32_e32 v68, v68, v70
	v_add_f32_e32 v69, v69, v71
	v_mov_b32_e32 v70, v68
	v_mov_b32_e32 v71, v69
	s_nop 1
	v_permlane32_swap_b32_e32 v68, v70
	v_permlane32_swap_b32_e32 v69, v71
	v_add_f32_e32 v68, v68, v70
	v_add_f32_e32 v69, v69, v71
	s_nop 0
	v_pk_fma_f32 v[68:69], v[68:69], s[0:1], v[196:197] op_sel_hi:[1,0,0]
	s_mov_b32 s0, 0x800000
	v_mul_f32_e32 v1, 0x4b800000, v68
	v_cmp_gt_f32_e32 vcc, s0, v68
	v_cmp_gt_f32_e64 s[0:1], s0, v69
	s_nop 0
	v_cndmask_b32_e32 v1, v68, v1, vcc
	v_rsq_f32_e32 v68, v1
	v_mul_f32_e32 v1, 0x4b800000, v69
	v_cndmask_b32_e64 v1, v69, v1, s[0:1]
	v_rsq_f32_e32 v69, v1
	s_nop 0
	v_pk_mul_f32 v[70:71], v[68:69], s[30:31] op_sel_hi:[1,0]
	s_nop 0
	v_cndmask_b32_e64 v153, v69, v71, s[0:1]
	v_cndmask_b32_e32 v152, v68, v70, vcc
	v_pk_mul_f32 v[68:69], v[184:185], v[152:153]
	v_mov_b32_e32 v70, v5
	v_pk_fma_f32 v[124:125], v[6:7], v[68:69], v[2:3] op_sel_hi:[0,1,0]
	v_pk_mul_f32 v[68:69], v[128:129], v[152:153]
	v_pk_mul_f32 v[74:75], v[74:75], v[152:153]
	v_pk_fma_f32 v[126:127], v[6:7], v[68:69], v[2:3] op_sel:[1,0,1]
	v_pk_mul_f32 v[68:69], v[186:187], v[152:153]
	v_max3_f32 v71, |v125|, 0, |v127|
	v_pk_fma_f32 v[128:129], v[8:9], v[68:69], v[4:5] op_sel_hi:[0,1,0]
	v_pk_mul_f32 v[68:69], v[130:131], v[152:153]
	v_max3_f32 v1, |v124|, 0, |v126|
	v_pk_fma_f32 v[130:131], v[34:35], v[68:69], v[70:71] op_sel_hi:[0,1,0]
	v_pk_mul_f32 v[68:69], v[180:181], v[152:153]
	v_max3_f32 v34, v71, |v129|, |v131|
	v_pk_fma_f32 v[112:113], v[14:15], v[68:69], v[10:11] op_sel_hi:[0,1,0]
	v_pk_mul_f32 v[68:69], v[116:117], v[152:153]
	v_mov_b32_e32 v70, v13
	v_pk_fma_f32 v[114:115], v[14:15], v[68:69], v[10:11] op_sel:[1,0,1]
	v_pk_mul_f32 v[68:69], v[120:121], v[152:153]
	v_max3_f32 v71, v34, |v113|, |v115|
	v_pk_fma_f32 v[118:119], v[16:17], v[68:69], v[12:13] op_sel_hi:[0,1,0]
	v_pk_mul_f32 v[68:69], v[122:123], v[152:153]
	v_mov_b32_e32 v34, v17
	v_pk_fma_f32 v[122:123], v[34:35], v[68:69], v[70:71] op_sel_hi:[0,1,0]
	v_pk_mul_f32 v[68:69], v[176:177], v[152:153]
	v_max3_f32 v34, v71, |v119|, |v123|
	v_pk_fma_f32 v[108:109], v[22:23], v[68:69], v[18:19] op_sel_hi:[0,1,0]
	v_pk_mul_f32 v[68:69], v[178:179], v[152:153]
; __device__ __forceinline__ unsigned pack_i8x4(float a, float b, float c, float d, float inv) { return q8u(a, inv) | (q8u(b, inv) << 8) | (q8u(c, inv) << 16) | (q8u(d, inv) << 24); }
; __device__ __forceinline__ float wave_max(float v) {
; #pragma unroll
;     for (int o = 1; o < 64; o <<= 1) v = fmaxf(v, __shfl_xor(v, o));
;     return v;
; __device__ __forceinline__ void phase_norm2(const Params& p, const Ctx& F, const int l) {
;     ...
;             for (int c = 0; c < 4; ++c) { vv[j][c] = vv[j][c] * rstd * A[j][c] + Bv[j][c]; am = __builtin_elementwise_max(am, __builtin_elementwise_abs(vv[j][c])); }
;         const float am0 = fmaxf(wave_max(am.x), 1e-20f), am1 = fmaxf(wave_max(am.y), 1e-20f), inv0 = 127.f / am0, inv1 = 127.f / am1;
;         unsigned* hn0 = (unsigned*)((signed char*)F.r1 + ((size_t)b * TPB + t) * DM) + F.lane;
;         unsigned* hn1 = (unsigned*)((signed char*)F.r1 + ((size_t)b * TPB + (two ? tB : t)) * DM) + F.lane;
; #pragma unroll
;         for (int j = 0; j < 8; ++j) { __builtin_nontemporal_store(pack_i8x4(vv[j][0].x, vv[j][1].x, vv[j][2].x, vv[j][3].x, inv0), hn0 + 64 * j);
;             if (two) __builtin_nontemporal_store(pack_i8x4(vv[j][0].y, vv[j][1].y, vv[j][2].y, vv[j][3].y, inv1), hn1 + 64 * j); }
;         if (F.lane == 0) { F.sah[b * TPB + t] = am0 * (1.f / 127.f); if (two) F.sah[b * TPB + tB] = am1 * (1.f / 127.f); }
	v_mov_b32_e32 v70, v21
	v_pk_fma_f32 v[110:111], v[22:23], v[68:69], v[18:19] op_sel:[1,0,1]
	v_pk_mul_f32 v[68:69], v[182:183], v[152:153]
	v_max3_f32 v71, v34, |v109|, |v111|
	v_pk_fma_f32 v[116:117], v[24:25], v[68:69], v[20:21] op_sel_hi:[0,1,0]
	v_pk_mul_f32 v[68:69], v[172:173], v[152:153]
	v_mov_b32_e32 v34, v25
	v_pk_fma_f32 v[120:121], v[34:35], v[68:69], v[70:71] op_sel_hi:[0,1,0]
	v_pk_mul_f32 v[68:69], v[174:175], v[152:153]
	v_max3_f32 v34, v71, |v117|, |v121|
	v_pk_fma_f32 v[96:97], v[30:31], v[68:69], v[26:27] op_sel_hi:[0,1,0]
	v_pk_mul_f32 v[68:69], v[100:101], v[152:153]
	v_mov_b32_e32 v70, v29
	v_pk_fma_f32 v[98:99], v[30:31], v[68:69], v[26:27] op_sel:[1,0,1]
	v_pk_mul_f32 v[68:69], v[104:105], v[152:153]
	v_max3_f32 v71, v34, |v97|, |v99|
	v_pk_fma_f32 v[102:103], v[32:33], v[68:69], v[28:29] op_sel_hi:[0,1,0]
	v_pk_mul_f32 v[68:69], v[106:107], v[152:153]
	v_mov_b32_e32 v34, v33
	v_pk_fma_f32 v[106:107], v[34:35], v[68:69], v[70:71] op_sel_hi:[0,1,0]
	v_pk_mul_f32 v[68:69], v[164:165], v[152:153]
	v_max3_f32 v1, v1, |v128|, |v130|
	v_pk_fma_f32 v[92:93], v[40:41], v[68:69], v[36:37] op_sel_hi:[0,1,0]
	v_pk_mul_f32 v[68:69], v[168:169], v[152:153]
	v_max3_f32 v1, v1, |v112|, |v114|
	v_max3_f32 v34, v71, |v103|, |v107|
	v_pk_fma_f32 v[94:95], v[40:41], v[68:69], v[36:37] op_sel:[1,0,1]
	v_pk_mul_f32 v[68:69], v[188:189], v[152:153]
	v_max3_f32 v1, v1, |v118|, |v122|
	v_max3_f32 v71, v34, |v93|, |v95|
	v_pk_fma_f32 v[100:101], v[42:43], v[68:69], v[38:39] op_sel_hi:[0,1,0]
	v_pk_mul_f32 v[68:69], v[166:167], v[152:153]
	v_mov_b32_e32 v34, v43
	v_mov_b32_e32 v70, v39
	v_max3_f32 v1, v1, |v108|, |v110|
	v_pk_fma_f32 v[104:105], v[34:35], v[68:69], v[70:71] op_sel_hi:[0,1,0]
	v_pk_mul_f32 v[68:69], v[170:171], v[152:153]
	v_max3_f32 v1, v1, |v116|, |v120|
	v_pk_fma_f32 v[80:81], v[48:49], v[68:69], v[44:45] op_sel_hi:[0,1,0]
	v_pk_mul_f32 v[68:69], v[84:85], v[152:153]
	v_max3_f32 v1, v1, |v96|, |v98|
	v_pk_fma_f32 v[82:83], v[48:49], v[68:69], v[44:45] op_sel:[1,0,1]
	v_pk_mul_f32 v[68:69], v[88:89], v[152:153]
	v_max3_f32 v1, v1, |v102|, |v106|
	v_pk_fma_f32 v[86:87], v[50:51], v[68:69], v[46:47] op_sel_hi:[0,1,0]
	v_pk_mul_f32 v[68:69], v[90:91], v[152:153]
	v_mov_b32_e32 v34, v51
	v_mov_b32_e32 v70, v47
	v_max3_f32 v1, v1, |v92|, |v94|
	v_pk_fma_f32 v[90:91], v[34:35], v[68:69], v[70:71] op_sel_hi:[0,1,0]
	v_pk_mul_f32 v[68:69], v[160:161], v[152:153]
	v_max3_f32 v1, v1, |v100|, |v104|
	v_pk_fma_f32 v[76:77], v[56:57], v[68:69], v[52:53] op_sel_hi:[0,1,0]
	v_pk_mul_f32 v[68:69], v[162:163], v[152:153]
	v_max3_f32 v1, v1, |v80|, |v82|
	v_pk_fma_f32 v[78:79], v[56:57], v[68:69], v[52:53] op_sel:[1,0,1]
	v_pk_mul_f32 v[68:69], v[198:199], v[152:153]
	v_max3_f32 v1, v1, |v86|, |v90|
	v_pk_fma_f32 v[84:85], v[58:59], v[68:69], v[54:55] op_sel_hi:[0,1,0]
	v_pk_mul_f32 v[68:69], v[156:157], v[152:153]
	v_mov_b32_e32 v34, v59
	v_mov_b32_e32 v70, v55
	v_max3_f32 v154, v71, |v101|, |v105|
	v_max3_f32 v1, v1, |v76|, |v78|
	v_pk_fma_f32 v[88:89], v[34:35], v[68:69], v[70:71] op_sel_hi:[0,1,0]
	v_pk_mul_f32 v[68:69], v[158:159], v[152:153]
	v_pk_mul_f32 v[70:71], v[72:73], v[152:153]
	v_max3_f32 v1, v1, |v84|, |v88|
	v_pk_fma_f32 v[68:69], v[60:61], v[68:69], v[64:65] op_sel_hi:[0,1,0]
	v_pk_fma_f32 v[70:71], v[60:61], v[70:71], v[64:65] op_sel:[1,0,1]
	v_pk_mul_f32 v[72:73], v[200:201], v[152:153]
	v_mov_b32_e32 v34, v63
	v_mov_b32_e32 v152, v67
	v_max3_f32 v1, v1, |v68|, |v70|
	v_pk_fma_f32 v[72:73], v[62:63], v[72:73], v[66:67] op_sel_hi:[0,1,0]
	v_pk_fma_f32 v[74:75], v[34:35], v[74:75], v[152:153] op_sel_hi:[0,1,0]
	v_max3_f32 v1, v1, |v72|, |v74|
	v_max3_f32 v152, v154, |v81|, |v83|
	v_max3_f32 v152, v152, |v87|, |v91|
	v_max3_f32 v152, v152, |v77|, |v79|
	v_max3_f32 v152, v152, |v85|, |v89|
	v_max3_f32 v152, v152, |v69|, |v71|
	s_nop 1
	v_max_f32_dpp v1, v1, v1 quad_perm:[1,0,3,2] row_mask:0xf bank_mask:0xf
	v_max3_f32 v152, v152, |v73|, |v75|
	s_nop 1
	v_max_f32_dpp v1, v1, v1 quad_perm:[2,3,0,1] row_mask:0xf bank_mask:0xf
	s_nop 1
	v_max_f32_dpp v152, v152, v152 quad_perm:[1,0,3,2] row_mask:0xf bank_mask:0xf
	s_nop 1
	v_max_f32_dpp v1, v1, v1 row_half_mirror row_mask:0xf bank_mask:0xf
	s_nop 1
	v_max_f32_dpp v152, v152, v152 quad_perm:[2,3,0,1] row_mask:0xf bank_mask:0xf
	s_nop 1
	v_max_f32_dpp v1, v1, v1 row_mirror row_mask:0xf bank_mask:0xf
	s_nop 1
	v_max_f32_dpp v152, v152, v152 row_half_mirror row_mask:0xf bank_mask:0xf
	v_mov_b32_e32 v34, v1
	s_nop 1
	v_permlane16_swap_b32_e32 v1, v34
	v_max_f32_e32 v1, v1, v34
	s_nop 1
	v_max_f32_dpp v152, v152, v152 row_mirror row_mask:0xf bank_mask:0xf
	v_mov_b32_e32 v34, v1
	s_nop 1
	v_permlane32_swap_b32_e32 v1, v34
	v_max3_f32 v157, v1, v34, s53
	v_mov_b32_e32 v153, v152
	s_nop 1
	v_permlane16_swap_b32_e32 v152, v153
	v_max_f32_e32 v1, v153, v153
	v_max_f32_e32 v1, v152, v1
	v_div_scale_f32 v152, s[0:1], v157, v157, s54
	v_rcp_f32_e32 v153, v152
	v_mov_b32_e32 v34, v1
	s_nop 1
	v_permlane32_swap_b32_e32 v1, v34
	v_max3_f32 v156, v1, v34, s53
	v_fma_f32 v1, -v152, v153, 1.0
	v_fmac_f32_e32 v153, v1, v153
	v_div_scale_f32 v1, vcc, s54, v157, s54
	v_mul_f32_e32 v34, v1, v153
	v_fma_f32 v154, -v152, v34, v1
	v_fmac_f32_e32 v34, v154, v153
	v_fma_f32 v1, -v152, v34, v1
	v_div_scale_f32 v152, s[0:1], v156, v156, s54
	v_rcp_f32_e32 v154, v152
	v_div_fmas_f32 v1, v1, v153, v34
	v_div_fixup_f32 v159, v1, v157, s54
	v_mul_f32_e32 v160, v128, v159
	v_fma_f32 v1, -v152, v154, 1.0
	v_fmac_f32_e32 v154, v1, v154
	v_div_scale_f32 v1, vcc, s54, v156, s54
	v_mul_f32_e32 v34, v1, v154
	v_fma_f32 v153, -v152, v34, v1
	v_fmac_f32_e32 v34, v153, v154
	v_fma_f32 v1, -v152, v34, v1
	v_div_fmas_f32 v1, v1, v154, v34
	v_mul_f32_e32 v34, v126, v159
	v_div_fixup_f32 v158, v1, v156, s54
	v_mul_f32_e32 v1, v124, v159
	v_rndne_f32_e32 v34, v34
	v_rndne_f32_e32 v160, v160
	v_mul_f32_e32 v161, v130, v159
	v_rndne_f32_e32 v1, v1
	v_cvt_i32_f32_e32 v34, v34
	v_cvt_i32_f32_e32 v160, v160
	v_rndne_f32_e32 v161, v161
	v_cvt_i32_f32_e32 v1, v1
	v_cvt_i32_f32_e32 v161, v161
	v_med3_i32 v34, v34, s80, v218
	v_med3_i32 v160, v160, s80, v218
	v_med3_i32 v1, v1, s80, v218
	v_lshlrev_b32_e32 v34, 8, v34
	v_lshlrev_b32_e32 v160, 16, v160
	v_med3_i32 v161, v161, s80, v218
	v_and_b32_e32 v34, 0xff00, v34
	v_and_b32_e32 v160, 0xff0000, v160
	v_perm_b32 v1, v161, v1, s81
	v_or3_b32 v1, v1, v34, v160
	v_cndmask_b32_e64 v34, 0, 1, s[8:9]
	v_lshl_add_u64 v[154:155], v[136:137], 0, s[12:13]
	v_lshl_add_u64 v[152:153], v[136:137], 0, s[14:15]
	v_cmp_ne_u32_e64 s[0:1], 1, v34
	s_andn2_b64 vcc, exec, s[8:9]
	global_store_dword v[154:155], v1, off nt
	s_cbranch_vccnz .LBB0_920
; __device__ __forceinline__ unsigned pack_i8x4(float a, float b, float c, float d, float inv) { return q8u(a, inv) | (q8u(b, inv) << 8) | (q8u(c, inv) << 16) | (q8u(d, inv) << 24); }
; __device__ __forceinline__ void phase_norm2(const Params& p, const Ctx& F, const int l) {
;     ...
;         for (int j = 0; j < 8; ++j) { __builtin_nontemporal_store(pack_i8x4(vv[j][0].x, vv[j][1].x, vv[j][2].x, vv[j][3].x, inv0), hn0 + 64 * j);
;             if (two) __builtin_nontemporal_store(pack_i8x4(vv[j][0].y, vv[j][1].y, vv[j][2].y, vv[j][3].y, inv1), hn1 + 64 * j); }
;         if (F.lane == 0) { F.sah[b * TPB + t] = am0 * (1.f / 127.f); if (two) F.sah[b * TPB + tB] = am1 * (1.f / 127.f); }
	v_mul_f32_e32 v160, v127, v158
	v_mul_f32_e32 v161, v129, v158
	v_mul_f32_e32 v1, v125, v158
	v_rndne_f32_e32 v160, v160
	v_rndne_f32_e32 v161, v161
	v_mul_f32_e32 v162, v131, v158
	v_rndne_f32_e32 v1, v1
	v_cvt_i32_f32_e32 v160, v160
	v_cvt_i32_f32_e32 v161, v161
	v_rndne_f32_e32 v162, v162
	v_cvt_i32_f32_e32 v1, v1
	v_cvt_i32_f32_e32 v162, v162
	v_med3_i32 v160, v160, s80, v218
	v_med3_i32 v161, v161, s80, v218
	v_med3_i32 v1, v1, s80, v218
	v_lshlrev_b32_e32 v160, 8, v160
	v_lshlrev_b32_e32 v161, 16, v161
	v_med3_i32 v162, v162, s80, v218
	v_and_b32_e32 v160, 0xff00, v160
	v_and_b32_e32 v161, 0xff0000, v161
	v_perm_b32 v1, v162, v1, s81
	v_or3_b32 v1, v1, v160, v161
	global_store_dword v[152:153], v1, off nt
